# baseline (speedup 1.0000x reference)
_Z6k_prepPKfS0_PfS1_PdS2_PtS3_S3_:
	s_lshl_b32 s12, s2, 4
	s_and_b32 s12, s12, 48
	s_bfe_u32 s13, s2, 0x40003
	s_lshr_b32 s3, s2, 2
	s_or_b32 s19, s12, s13
	s_and_b32 s3, s3, 32
	s_lshl_b32 s12, s19, 6
	s_load_dwordx8 s[4:11], s[0:1], 0x0
	s_load_dwordx4 s[28:31], s[0:1], 0x38
	s_load_dwordx4 s[24:27], s[0:1], 0x20
	s_bfe_u32 s20, s2, 0x10002
	s_or_b32 s18, s12, s3
	s_and_b32 s14, s2, 0x100
	s_bitcmp1_b32 s2, 8
	s_cselect_b64 s[12:13], -1, 0
	s_cmp_eq_u32 s14, 0
	s_cselect_b64 s[14:15], -1, 0
	s_and_b64 s[16:17], s[14:15], exec
	s_waitcnt lgkmcnt(0)
	s_cselect_b32 s5, s5, s7
	s_cselect_b32 s4, s4, s6
	s_lshl_b32 s6, s20, 21
	s_add_u32 s4, s4, s6
	s_addc_u32 s5, s5, 0
	s_lshl_b32 s6, s18, 2
	s_add_u32 s4, s4, s6
	v_and_b32_e32 v20, 31, v0
	s_addc_u32 s5, s5, 0
	v_lshrrev_b32_e32 v1, 5, v0
	v_lshlrev_b32_e32 v10, 2, v20
	v_mov_b32_e32 v11, 0
	v_lshl_add_u64 v[2:3], s[4:5], 0, v[10:11]
	v_lshlrev_b32_e32 v4, 18, v1
	v_mov_b32_e32 v5, v11
	v_lshl_add_u64 v[2:3], v[2:3], 0, v[4:5]
	s_movk_i32 s4, 0x4000
	v_add_co_u32_e32 v4, vcc, s4, v2
	s_mov_b32 s4, 0x8000
	s_nop 0
	v_addc_co_u32_e32 v5, vcc, 0, v3, vcc
	v_add_co_u32_e32 v6, vcc, s4, v2
	s_mov_b32 s4, 0xc000
	s_nop 0
	v_addc_co_u32_e32 v7, vcc, 0, v3, vcc
	v_add_co_u32_e32 v8, vcc, s4, v2
	s_mov_b32 s4, 0x10000
	s_nop 0
	v_addc_co_u32_e32 v9, vcc, 0, v3, vcc
	v_add_co_u32_e32 v12, vcc, s4, v2
	s_mov_b32 s4, 0x14000
	s_nop 0
	v_addc_co_u32_e32 v13, vcc, 0, v3, vcc
	v_add_co_u32_e32 v14, vcc, s4, v2
	s_mov_b32 s4, 0x18000
	s_nop 0
	v_addc_co_u32_e32 v15, vcc, 0, v3, vcc
	v_add_co_u32_e32 v16, vcc, s4, v2
	s_mov_b32 s4, 0x1c000
	s_nop 0
	v_addc_co_u32_e32 v17, vcc, 0, v3, vcc
	v_add_co_u32_e32 v18, vcc, s4, v2
	s_mov_b32 s4, 0x20000
	s_nop 0
	v_addc_co_u32_e32 v19, vcc, 0, v3, vcc
	global_load_dword v21, v[2:3], off nt
	global_load_dword v22, v[4:5], off nt
	global_load_dword v23, v[6:7], off nt
	global_load_dword v24, v[8:9], off nt
	global_load_dword v25, v[12:13], off nt
	global_load_dword v26, v[14:15], off nt
	global_load_dword v27, v[16:17], off nt
	global_load_dword v28, v[18:19], off nt
	v_add_co_u32_e32 v4, vcc, s4, v2
	s_mov_b32 s4, 0x24000
	s_nop 0
	v_addc_co_u32_e32 v5, vcc, 0, v3, vcc
	v_add_co_u32_e32 v6, vcc, s4, v2
	s_mov_b32 s4, 0x28000
	s_nop 0
	v_addc_co_u32_e32 v7, vcc, 0, v3, vcc
	v_add_co_u32_e32 v8, vcc, s4, v2
	s_mov_b32 s4, 0x2c000
	s_nop 0
	v_addc_co_u32_e32 v9, vcc, 0, v3, vcc
	v_add_co_u32_e32 v12, vcc, s4, v2
	s_mov_b32 s4, 0x30000
	s_nop 0
	v_addc_co_u32_e32 v13, vcc, 0, v3, vcc
	global_load_dword v14, v[4:5], off nt
	global_load_dword v15, v[6:7], off nt
	global_load_dword v16, v[8:9], off nt
	global_load_dword v17, v[12:13], off nt
	v_add_co_u32_e32 v4, vcc, s4, v2
	s_mov_b32 s4, 0x34000
	s_nop 0
	v_addc_co_u32_e32 v5, vcc, 0, v3, vcc
	v_add_co_u32_e32 v6, vcc, s4, v2
	s_mov_b32 s4, 0x38000
	s_nop 0
	v_addc_co_u32_e32 v7, vcc, 0, v3, vcc
	v_add_co_u32_e32 v8, vcc, s4, v2
	s_mov_b32 s4, 0x3c000
	s_nop 0
	v_addc_co_u32_e32 v9, vcc, 0, v3, vcc
	v_add_co_u32_e32 v2, vcc, s4, v2
	global_load_dword v12, v[4:5], off nt
	global_load_dword v13, v[6:7], off nt
	global_load_dword v18, v[8:9], off nt
	v_addc_co_u32_e32 v3, vcc, 0, v3, vcc
	global_load_dword v6, v[2:3], off nt
	s_load_dwordx2 s[16:17], s[0:1], 0x30
	s_movk_i32 s4, 0x840
	v_mad_u32_u24 v7, v1, s4, v10
	v_cmp_gt_u32_e32 vcc, 32, v0
	s_waitcnt vmcnt(15)
	v_cvt_f64_f32_e32 v[2:3], v21
	s_waitcnt vmcnt(14)
	v_cvt_f64_f32_e32 v[4:5], v22
	v_mul_f64 v[4:5], v[4:5], v[4:5]
	v_fmac_f64_e32 v[4:5], v[2:3], v[2:3]
	s_waitcnt vmcnt(13)
	v_cvt_f64_f32_e32 v[2:3], v23
	v_fmac_f64_e32 v[4:5], v[2:3], v[2:3]
	s_waitcnt vmcnt(12)
	v_cvt_f64_f32_e32 v[2:3], v24
	v_fmac_f64_e32 v[4:5], v[2:3], v[2:3]
	s_waitcnt vmcnt(11)
	v_cvt_f64_f32_e32 v[2:3], v25
	v_fmac_f64_e32 v[4:5], v[2:3], v[2:3]
	s_waitcnt vmcnt(10)
	v_cvt_f64_f32_e32 v[2:3], v26
	v_fmac_f64_e32 v[4:5], v[2:3], v[2:3]
	s_waitcnt vmcnt(9)
	v_cvt_f64_f32_e32 v[2:3], v27
	v_fmac_f64_e32 v[4:5], v[2:3], v[2:3]
	s_waitcnt vmcnt(8)
	v_cvt_f64_f32_e32 v[2:3], v28
	v_fmac_f64_e32 v[4:5], v[2:3], v[2:3]
	ds_write2_b32 v7, v21, v22 offset1:33
	ds_write2_b32 v7, v23, v24 offset0:66 offset1:99
	ds_write2_b32 v7, v25, v26 offset0:132 offset1:165
	ds_write2_b32 v7, v27, v28 offset0:198 offset1:231
	v_add_u32_e32 v7, 0x400, v7
	s_waitcnt vmcnt(7)
	v_cvt_f64_f32_e32 v[2:3], v14
	v_fmac_f64_e32 v[4:5], v[2:3], v[2:3]
	s_waitcnt vmcnt(6)
	v_cvt_f64_f32_e32 v[2:3], v15
	v_fmac_f64_e32 v[4:5], v[2:3], v[2:3]
	s_waitcnt vmcnt(5)
	v_cvt_f64_f32_e32 v[2:3], v16
	v_fmac_f64_e32 v[4:5], v[2:3], v[2:3]
	s_waitcnt vmcnt(4)
	v_cvt_f64_f32_e32 v[2:3], v17
	v_fmac_f64_e32 v[4:5], v[2:3], v[2:3]
	ds_write2_b32 v7, v14, v15 offset0:8 offset1:41
	ds_write2_b32 v7, v16, v17 offset0:74 offset1:107
	s_waitcnt vmcnt(3)
	v_cvt_f64_f32_e32 v[2:3], v12
	v_fmac_f64_e32 v[4:5], v[2:3], v[2:3]
	s_waitcnt vmcnt(2)
	v_cvt_f64_f32_e32 v[2:3], v13
	v_fmac_f64_e32 v[4:5], v[2:3], v[2:3]
	s_waitcnt vmcnt(1)
	v_cvt_f64_f32_e32 v[2:3], v18
	v_fmac_f64_e32 v[4:5], v[2:3], v[2:3]
	s_waitcnt vmcnt(0)
	v_cvt_f64_f32_e32 v[2:3], v6
	v_fmac_f64_e32 v[4:5], v[2:3], v[2:3]
	v_lshlrev_b32_e32 v2, 3, v20
	v_lshl_or_b32 v2, v1, 8, v2
	ds_write2_b32 v7, v12, v13 offset0:140 offset1:173
	ds_write2_b32 v7, v18, v6 offset0:206 offset1:239
	ds_write_b64 v2, v[4:5] offset:16896
	s_waitcnt lgkmcnt(0)
	s_barrier
	s_and_saveexec_b64 s[4:5], vcc
	s_cbranch_execz .LBB0_2
	v_lshlrev_b32_e32 v10, 3, v0
	v_add_u32_e32 v12, 0x4000, v10
	v_add_u32_e32 v16, 0x4800, v10
	ds_read2_b64 v[2:5], v12 offset0:64 offset1:96
	ds_read2_b64 v[6:9], v12 offset0:128 offset1:160
	ds_read2_b64 v[12:15], v12 offset0:192 offset1:224
	ds_read2_b64 v[16:19], v16 offset1:32
	s_and_b64 s[6:7], s[14:15], exec
	s_waitcnt lgkmcnt(0)
	s_cselect_b32 s6, s25, s27
	s_cselect_b32 s7, s24, s26
	s_lshl_b32 s21, s20, 15
	s_add_u32 s7, s7, s21
	v_add_f64 v[2:3], v[2:3], v[4:5]
	v_add_f64 v[4:5], v[6:7], v[8:9]
	s_addc_u32 s21, s6, 0
	s_lshl_b32 s6, s18, 3
	v_add_f64 v[2:3], v[2:3], v[4:5]
	v_add_f64 v[4:5], v[12:13], v[14:15]
	v_add_f64 v[6:7], v[16:17], v[18:19]
	s_add_u32 s6, s7, s6
	v_add_f64 v[4:5], v[4:5], v[6:7]
	s_addc_u32 s7, s21, 0
	v_add_f64 v[2:3], v[2:3], v[4:5]
	global_store_dwordx2 v10, v[2:3], s[6:7]
.LBB0_2:
	s_or_b64 exec, exec, s[4:5]
	s_mov_b64 s[4:5], s[28:29]
	s_mov_b64 s[6:7], s[30:31]
	s_lshl_b32 s0, s20, 12
	s_or_b32 s18, s18, s0
	s_lshl_b32 s21, s18, 9
	s_and_b64 s[0:1], s[14:15], exec
	s_cselect_b32 s0, s8, s10
	v_lshlrev_b32_e32 v2, 2, v0
	s_cselect_b32 s1, s9, s11
	s_add_u32 s0, s0, s21
	v_and_b32_e32 v19, 0x7c, v2
	s_movk_i32 s10, 0x84
	v_lshlrev_b32_e32 v2, 2, v1
	s_addc_u32 s1, s1, 0
	s_bfe_u32 s15, s2, 0x30003
	v_mad_u32_u24 v4, v19, s10, v2
	s_add_i32 s14, s15, -4
	ds_read2_b32 v[2:3], v4 offset1:33
	ds_read2_b32 v[4:5], v4 offset0:66 offset1:99
	s_cmp_eq_u32 s14, 0
	v_lshlrev_b32_e32 v10, 2, v19
	s_cselect_b64 s[8:9], -1, 0
	s_cmp_gt_u32 s15, 4
	v_lshl_add_u64 v[8:9], s[0:1], 0, v[10:11]
	s_cselect_b32 s0, 1, 0
	s_cmp_gt_u32 s15, 3
	v_lshlrev_b32_e32 v12, 9, v1
	v_mov_b32_e32 v13, v11
	v_lshlrev_b32_e32 v10, 1, v19
	s_cselect_b32 s0, s0, -1
	v_lshl_add_u64 v[12:13], v[8:9], 0, v[12:13]
	v_lshl_add_u64 v[6:7], s[16:17], 0, v[10:11]
	s_mul_i32 s0, s0, 3
	s_mul_i32 s17, s20, 27
	s_waitcnt lgkmcnt(0)
	global_store_dwordx4 v[12:13], v[2:5], off
	v_or_b32_e32 v12, s18, v1
	v_mov_b32_e32 v13, v11
	v_cvt_pk_f16_f32 v2, v2, v3
	v_cndmask_b32_e64 v3, 0, 1, s[12:13]
	s_add_i32 s17, s17, s0
	v_cmp_ne_u32_e64 s[0:1], 1, v3
	s_andn2_b64 vcc, exec, s[12:13]
	v_lshlrev_b64 v[16:17], 8, v[12:13]
	s_cbranch_vccnz .LBB0_4
	v_lshl_add_u64 v[14:15], v[6:7], 0, v[16:17]
	s_mov_b64 s[12:13], 0
	s_mov_b64 s[10:11], -1
	global_store_dword v[14:15], v2, off
	s_branch .LBB0_5

	.amdhsa_kernel _Z6k_prepPKfS0_PfS1_PdS2_PtS3_S3_
		.amdhsa_group_segment_fixed_size 18944
		.amdhsa_private_segment_fixed_size 0
		.amdhsa_kernarg_size 72
		.amdhsa_user_sgpr_count 2
		.amdhsa_user_sgpr_dispatch_ptr 0
		.amdhsa_user_sgpr_queue_ptr 0
		.amdhsa_user_sgpr_kernarg_segment_ptr 1
		.amdhsa_user_sgpr_dispatch_id 0
		.amdhsa_user_sgpr_kernarg_preload_length 0
		.amdhsa_user_sgpr_kernarg_preload_offset 0
		.amdhsa_user_sgpr_private_segment_size 0
		.amdhsa_uses_dynamic_stack 0
		.amdhsa_enable_private_segment 0
		.amdhsa_system_sgpr_workgroup_id_x 1
		.amdhsa_system_sgpr_workgroup_id_y 0
		.amdhsa_system_sgpr_workgroup_id_z 0
		.amdhsa_system_sgpr_workgroup_info 0
		.amdhsa_system_vgpr_workitem_id 0
		.amdhsa_next_free_vgpr 29
		.amdhsa_next_free_sgpr 32
		.amdhsa_accum_offset 32
		.amdhsa_reserve_vcc 1
		.amdhsa_float_round_mode_32 0
		.amdhsa_float_round_mode_16_64 0
		.amdhsa_float_denorm_mode_32 3
		.amdhsa_float_denorm_mode_16_64 3
		.amdhsa_dx10_clamp 1
		.amdhsa_ieee_mode 1
		.amdhsa_fp16_overflow 0
		.amdhsa_tg_split 0
		.amdhsa_exception_fp_ieee_invalid_op 0
		.amdhsa_exception_fp_denorm_src 0
		.amdhsa_exception_fp_ieee_div_zero 0
		.amdhsa_exception_fp_ieee_overflow 0
		.amdhsa_exception_fp_ieee_underflow 0
		.amdhsa_exception_fp_ieee_inexact 0
		.amdhsa_exception_int_div_zero 0
	.end_amdhsa_kernel

_Z9k_coarse2PKtS0_PKdS2_Pf:
	s_and_b32 s3, s2, 7
	s_mul_i32 s3, s3, 48
	s_lshr_b32 s2, s2, 3
	s_load_dwordx4 s[4:7], s[0:1], 0x0
	s_load_dwordx2 s[38:39], s[0:1], 0x20
	s_add_i32 s3, s3, s2
	s_mul_hi_u32 s10, s3, 0x55555556
	s_mul_i32 s2, s10, 3
	s_sub_i32 s26, s3, s2
	s_mul_hi_u32 s2, s3, 0x2aaaaaab
	s_lshr_b32 s22, s2, 5
	v_cmp_lt_u32_e32 vcc, 63, v0
	v_lshlrev_b32_e32 v1, 3, v0
	s_and_saveexec_b64 s[2:3], vcc
	s_xor_b64 s[2:3], exec, s[2:3]
	s_lshl_b32 s8, s22, 12
	s_not_b32 s9, s26
	v_lshlrev_b32_e32 v74, 3, v0
	v_mov_b32_e32 v72, s9
	v_mov_b32_e32 v83, s8
	s_or_saveexec_b64 s[2:3], s[2:3]
	s_load_dwordx2 s[8:9], s[0:1], 0x10
	s_add_i32 s12, s26, 1
	s_xor_b64 exec, exec, s[2:3]
	s_cbranch_execz .LBB1_4
	s_load_dwordx2 s[14:15], s[0:1], 0x18
	s_lshl_b32 s11, s22, 12
	v_and_or_b32 v23, v1, 56, s11
	v_and_or_b32 v22, v0, 56, 4
	v_or_b32_e32 v24, 4, v23
	s_not_b32 s13, s26
	v_add_lshl_u32 v2, v22, s13, 6
	v_add_u32_e32 v25, s13, v24
	v_or_b32_e32 v4, v25, v2
	v_mov_b32_e32 v5, 0
	s_waitcnt lgkmcnt(0)
	v_lshl_add_u64 v[6:7], v[4:5], 3, s[14:15]
	v_add_u32_e32 v4, v23, v2
	v_mov_b32_e32 v3, v5
	v_lshl_add_u64 v[8:9], v[4:5], 3, s[14:15]
	v_add_u32_e32 v4, s12, v23
	v_lshlrev_b32_e32 v10, 6, v22
	v_lshl_add_u64 v[2:3], v[4:5], 0, v[2:3]
	v_or_b32_e32 v12, v25, v10
	v_mov_b32_e32 v13, v5
	v_lshl_add_u64 v[2:3], v[2:3], 3, s[14:15]
	v_lshl_add_u64 v[12:13], v[12:13], 3, s[14:15]
	global_load_dwordx2 v[14:15], v[6:7], off
	global_load_dwordx2 v[16:17], v[8:9], off offset:32
	global_load_dwordx2 v[18:19], v[2:3], off offset:32
	global_load_dwordx2 v[20:21], v[12:13], off
	v_add_lshl_u32 v8, v22, s12, 6
	v_mov_b32_e32 v11, v5
	v_or_b32_e32 v2, v23, v10
	v_mov_b32_e32 v3, v5
	v_add_u32_e32 v6, v25, v8
	v_add_u32_e32 v8, v24, v8
	v_lshl_add_u64 v[2:3], v[2:3], 3, s[14:15]
	v_lshl_add_u64 v[4:5], v[4:5], 0, v[10:11]
	v_ashrrev_i32_e32 v7, 31, v6
	v_ashrrev_i32_e32 v9, 31, v8
	v_lshl_add_u64 v[4:5], v[4:5], 3, s[14:15]
	v_lshl_add_u64 v[6:7], v[6:7], 3, s[14:15]
	v_lshl_add_u64 v[10:11], v[8:9], 3, s[14:15]
	global_load_dwordx2 v[12:13], v[2:3], off offset:32
	global_load_dwordx2 v[22:23], v[4:5], off offset:32
	global_load_dwordx2 v[24:25], v[6:7], off
	global_load_dwordx2 v[26:27], v[10:11], off
	v_add_u32_e32 v2, s12, v8
	v_ashrrev_i32_e32 v3, 31, v2
	v_lshl_add_u64 v[2:3], v[2:3], 3, s[14:15]
	global_load_dwordx2 v[2:3], v[2:3], off
	s_mov_b32 s14, 0
	s_brev_b32 s15, 8
	v_mov_b32_e32 v6, 0x100
	v_mov_b32_e32 v7, 0xffffff80
	v_mov_b32_e32 v10, 0x260
	s_mov_b32 s16, 0x812dea11
	s_mov_b32 s17, 0x3d719799
	v_mov_b32_e32 v83, s11
	v_mov_b32_e32 v72, s13
	v_mov_b32_e32 v74, v1
	s_waitcnt vmcnt(8)
	v_add_f64 v[4:5], v[14:15], 0
	s_waitcnt vmcnt(7)
	v_add_f64 v[4:5], v[4:5], v[16:17]
	s_waitcnt vmcnt(6)
	v_add_f64 v[4:5], v[4:5], v[18:19]
	s_waitcnt vmcnt(5)
	v_add_f64 v[4:5], v[4:5], v[20:21]
	s_waitcnt vmcnt(4)
	v_add_f64 v[4:5], v[4:5], v[12:13]
	s_waitcnt vmcnt(3)
	v_add_f64 v[4:5], v[4:5], v[22:23]
	s_waitcnt vmcnt(2)
	v_add_f64 v[4:5], v[4:5], v[24:25]
	s_waitcnt vmcnt(1)
	v_add_f64 v[4:5], v[4:5], v[26:27]
	v_lshlrev_b32_e32 v12, 2, v0
	s_waitcnt vmcnt(0)
	v_add_f64 v[2:3], v[4:5], v[2:3]
	v_cmp_gt_f64_e32 vcc, s[14:15], v[2:3]
	s_nop 1
	v_cndmask_b32_e32 v4, 0, v6, vcc
	v_ldexp_f64 v[2:3], v[2:3], v4
	v_rsq_f64_e32 v[4:5], v[2:3]
	v_cndmask_b32_e32 v11, 0, v7, vcc
	v_cmp_class_f64_e32 vcc, v[2:3], v10
	v_mul_f64 v[6:7], v[2:3], v[4:5]
	v_mul_f64 v[4:5], v[4:5], 0.5
	v_fma_f64 v[8:9], -v[4:5], v[6:7], 0.5
	v_fmac_f64_e32 v[6:7], v[6:7], v[8:9]
	v_fmac_f64_e32 v[4:5], v[4:5], v[8:9]
	v_fma_f64 v[8:9], -v[6:7], v[6:7], v[2:3]
	v_fmac_f64_e32 v[6:7], v[8:9], v[4:5]
	v_fma_f64 v[8:9], -v[6:7], v[6:7], v[2:3]
	v_fmac_f64_e32 v[6:7], v[8:9], v[4:5]
	v_ldexp_f64 v[4:5], v[6:7], v11
	v_cndmask_b32_e32 v3, v5, v3, vcc
	v_cndmask_b32_e32 v2, v4, v2, vcc
	v_max_f64 v[2:3], v[2:3], s[16:17]
	v_div_scale_f64 v[4:5], s[14:15], v[2:3], v[2:3], 1.0
	v_rcp_f64_e32 v[6:7], v[4:5]
	v_div_scale_f64 v[8:9], vcc, 1.0, v[2:3], 1.0
	v_fma_f64 v[10:11], -v[4:5], v[6:7], 1.0
	v_fmac_f64_e32 v[6:7], v[6:7], v[10:11]
	v_fma_f64 v[10:11], -v[4:5], v[6:7], 1.0
	v_fmac_f64_e32 v[6:7], v[6:7], v[10:11]
	v_mul_f64 v[10:11], v[8:9], v[6:7]
	v_fma_f64 v[4:5], -v[4:5], v[10:11], v[8:9]
	v_div_fmas_f64 v[4:5], v[4:5], v[6:7], v[10:11]
	v_div_fixup_f64 v[2:3], v[4:5], v[2:3], 1.0
	v_cvt_f32_f64_e32 v2, v[2:3]
	ds_write_b32 v12, v2

.LBB1_46:
	s_mov_b64 s[0:1], s[38:39]
	s_and_b64 vcc, exec, s[20:21]
	s_waitcnt lgkmcnt(0)
	s_barrier
	s_cbranch_vccnz .LBB1_48
	s_waitcnt vmcnt(0)
	v_mul_u32_u24_e32 v0, 0x110, v26
	v_add_u32_e32 v15, v16, v0
	ds_read_b128 v[0:3], v15 offset:19040
	ds_read_b128 v[4:7], v12 offset:816
	ds_read_b128 v[8:11], v12 offset:848
	ds_read_b128 v[18:21], v15 offset:19072
	s_waitcnt lgkmcnt(2)
	v_mfma_f32_32x32x16_f16 a[0:15], v[0:3], v[4:7], a[0:15]
	s_waitcnt lgkmcnt(0)
	v_mfma_f32_32x32x16_f16 a[0:15], v[18:21], v[8:11], a[0:15]
	ds_read_b128 v[0:3], v15 offset:19104
	ds_read_b128 v[4:7], v12 offset:880
	ds_read_b128 v[8:11], v12 offset:912
	ds_read_b128 v[18:21], v15 offset:19136
	s_waitcnt lgkmcnt(2)
	v_mfma_f32_32x32x16_f16 a[0:15], v[0:3], v[4:7], a[0:15]
	s_waitcnt lgkmcnt(0)
	v_mfma_f32_32x32x16_f16 a[0:15], v[18:21], v[8:11], a[0:15]
	ds_read_b128 v[0:3], v15 offset:19168
	ds_read_b128 v[4:7], v12 offset:944
	ds_read_b128 v[8:11], v12 offset:976
	ds_read_b128 v[18:21], v15 offset:19200
	s_waitcnt lgkmcnt(2)
	v_mfma_f32_32x32x16_f16 a[0:15], v[0:3], v[4:7], a[0:15]
	s_waitcnt lgkmcnt(0)
	v_mfma_f32_32x32x16_f16 a[0:15], v[18:21], v[8:11], a[0:15]
	ds_read_b128 v[0:3], v15 offset:19232
	ds_read_b128 v[4:7], v12 offset:1008
	ds_read_b128 v[8:11], v12 offset:1040
	ds_read_b128 v[18:21], v15 offset:19264
	s_waitcnt lgkmcnt(2)
	v_mfma_f32_32x32x16_f16 a[0:15], v[0:3], v[4:7], a[0:15]
	s_waitcnt lgkmcnt(0)
	v_mfma_f32_32x32x16_f16 a[0:15], v[18:21], v[8:11], a[0:15]
	ds_read_b128 v[0:3], v15 offset:36448
	ds_read_b128 v[4:7], v13 offset:816
	ds_read_b128 v[8:11], v13 offset:848
	ds_read_b128 v[18:21], v15 offset:36480
	s_waitcnt lgkmcnt(2)
	v_mfma_f32_32x32x16_f16 a[0:15], v[0:3], v[4:7], a[0:15]
	s_waitcnt lgkmcnt(0)
	v_mfma_f32_32x32x16_f16 a[0:15], v[18:21], v[8:11], a[0:15]
	ds_read_b128 v[0:3], v15 offset:36512
	ds_read_b128 v[4:7], v13 offset:880
	ds_read_b128 v[8:11], v13 offset:912
	ds_read_b128 v[18:21], v15 offset:36544
	s_waitcnt lgkmcnt(2)
	v_mfma_f32_32x32x16_f16 a[0:15], v[0:3], v[4:7], a[0:15]
	s_waitcnt lgkmcnt(0)
	v_mfma_f32_32x32x16_f16 a[0:15], v[18:21], v[8:11], a[0:15]
	ds_read_b128 v[0:3], v15 offset:36576
	ds_read_b128 v[4:7], v13 offset:944
	ds_read_b128 v[8:11], v13 offset:976
	ds_read_b128 v[18:21], v15 offset:36608
	s_waitcnt lgkmcnt(2)
	v_mfma_f32_32x32x16_f16 a[0:15], v[0:3], v[4:7], a[0:15]
	s_waitcnt lgkmcnt(0)
	v_mfma_f32_32x32x16_f16 a[0:15], v[18:21], v[8:11], a[0:15]
	ds_read_b128 v[0:3], v15 offset:36640
	ds_read_b128 v[4:7], v13 offset:1008
	ds_read_b128 v[8:11], v13 offset:1040
	ds_read_b128 v[18:21], v15 offset:36672
	s_waitcnt lgkmcnt(2)
	v_mfma_f32_32x32x16_f16 a[0:15], v[0:3], v[4:7], a[0:15]
	s_waitcnt lgkmcnt(0)
	v_mfma_f32_32x32x16_f16 a[0:15], v[18:21], v[8:11], a[0:15]
	ds_read_b128 v[0:3], v15 offset:53856
	ds_read_b128 v[4:7], v14 offset:816
	ds_read_b128 v[8:11], v14 offset:848
	ds_read_b128 v[18:21], v15 offset:53888
	s_waitcnt lgkmcnt(2)
	v_mfma_f32_32x32x16_f16 a[0:15], v[0:3], v[4:7], a[0:15]
	s_waitcnt lgkmcnt(0)
	v_mfma_f32_32x32x16_f16 a[0:15], v[18:21], v[8:11], a[0:15]
	ds_read_b128 v[0:3], v15 offset:53920
	ds_read_b128 v[4:7], v14 offset:880
	ds_read_b128 v[8:11], v14 offset:912
	ds_read_b128 v[18:21], v15 offset:53952
	s_waitcnt lgkmcnt(2)
	v_mfma_f32_32x32x16_f16 a[0:15], v[0:3], v[4:7], a[0:15]
	s_waitcnt lgkmcnt(0)
	v_mfma_f32_32x32x16_f16 a[0:15], v[18:21], v[8:11], a[0:15]
	ds_read_b128 v[0:3], v15 offset:53984
	ds_read_b128 v[4:7], v14 offset:944
	ds_read_b128 v[8:11], v14 offset:976
	ds_read_b128 v[18:21], v15 offset:54016
	s_waitcnt lgkmcnt(2)
	v_mfma_f32_32x32x16_f16 a[0:15], v[0:3], v[4:7], a[0:15]
	s_waitcnt lgkmcnt(0)
	v_mfma_f32_32x32x16_f16 a[0:15], v[18:21], v[8:11], a[0:15]
	ds_read_b128 v[0:3], v15 offset:54048
	ds_read_b128 v[4:7], v14 offset:1008
	ds_read_b128 v[8:11], v15 offset:54080
	ds_read_b128 v[12:15], v14 offset:1040
	s_waitcnt lgkmcnt(2)
	v_mfma_f32_32x32x16_f16 a[0:15], v[0:3], v[4:7], a[0:15]
	s_waitcnt lgkmcnt(0)
	v_mfma_f32_32x32x16_f16 a[0:15], v[8:11], v[12:15], a[0:15]

	.amdhsa_kernel _Z9k_coarse2PKtS0_PKdS2_Pf
		.amdhsa_group_segment_fixed_size 256
		.amdhsa_private_segment_fixed_size 0
		.amdhsa_kernarg_size 40
		.amdhsa_user_sgpr_count 2
		.amdhsa_user_sgpr_dispatch_ptr 0
		.amdhsa_user_sgpr_queue_ptr 0
		.amdhsa_user_sgpr_kernarg_segment_ptr 1
		.amdhsa_user_sgpr_dispatch_id 0
		.amdhsa_user_sgpr_kernarg_preload_length 0
		.amdhsa_user_sgpr_kernarg_preload_offset 0
		.amdhsa_user_sgpr_private_segment_size 0
		.amdhsa_uses_dynamic_stack 0
		.amdhsa_enable_private_segment 0
		.amdhsa_system_sgpr_workgroup_id_x 1
		.amdhsa_system_sgpr_workgroup_id_y 0
		.amdhsa_system_sgpr_workgroup_id_z 0
		.amdhsa_system_sgpr_workgroup_info 0
		.amdhsa_system_vgpr_workitem_id 0
		.amdhsa_next_free_vgpr 156
		.amdhsa_next_free_sgpr 40
		.amdhsa_accum_offset 140
		.amdhsa_reserve_vcc 1
		.amdhsa_float_round_mode_32 0
		.amdhsa_float_round_mode_16_64 0
		.amdhsa_float_denorm_mode_32 3
		.amdhsa_float_denorm_mode_16_64 3
		.amdhsa_dx10_clamp 1
		.amdhsa_ieee_mode 1
		.amdhsa_fp16_overflow 0
		.amdhsa_tg_split 0
		.amdhsa_exception_fp_ieee_invalid_op 0
		.amdhsa_exception_fp_denorm_src 0
		.amdhsa_exception_fp_ieee_div_zero 0
		.amdhsa_exception_fp_ieee_overflow 0
		.amdhsa_exception_fp_ieee_underflow 0
		.amdhsa_exception_fp_ieee_inexact 0
		.amdhsa_exception_int_div_zero 0
	.end_amdhsa_kernel

_Z10k_transferPKtS0_PKfPKiS2_S4_PfS5_S5_:
	s_load_dwordx4 s[16:19], s[0:1], 0x18
	s_load_dwordx2 s[14:15], s[0:1], 0x28
	s_load_dwordx2 s[28:29], s[0:1], 0x40
	s_load_dwordx4 s[32:35], s[0:1], 0x30
	s_load_dwordx4 s[36:39], s[0:1], 0x0
	s_load_dwordx2 s[30:31], s[0:1], 0x10
	s_mov_b64 s[4:5], -1
	s_cmpk_gt_i32 s2, 0x3ff
	v_cmp_gt_u32_e64 s[10:11], 64, v0
	s_cbranch_scc0 .LBB3_31
	s_cmpk_gt_u32 s2, 0x7ff
	s_cbranch_scc0 .LBB3_14
	s_add_i32 s12, s2, 0xfffff800
	s_lshr_b32 s3, s12, 4
	s_lshl_b32 s8, s3, 3
	s_waitcnt lgkmcnt(0)
	s_mov_b64 s[4:5], s[36:37]
	s_load_dwordx2 s[6:7], s[14:15], s8 offset:0x0
	s_and_saveexec_b64 s[8:9], s[10:11]
	s_cbranch_execz .LBB3_4
	v_lshl_or_b32 v2, s3, 6, v0
	v_mov_b32_e32 v3, 0
	v_lshlrev_b64 v[2:3], 2, v[2:3]
	v_lshl_add_u64 v[4:5], s[16:17], 0, v[2:3]
	v_lshl_add_u64 v[2:3], s[18:19], 0, v[2:3]
	global_load_dword v1, v[4:5], off
	global_load_dword v6, v[2:3], off
	v_lshlrev_b32_e32 v2, 2, v0
	v_add_u32_e32 v2, 0x50, v2
	s_waitcnt vmcnt(0)
	ds_write2st64_b32 v2, v1, v6 offset0:70 offset1:71

.LBB3_10:
	s_or_b64 exec, exec, s[4:5]
	s_movk_i32 s4, 0x200
	v_cmp_gt_u32_e32 vcc, s4, v0
	s_waitcnt lgkmcnt(0)
	s_barrier
	s_and_saveexec_b64 s[22:23], vcc
	s_cbranch_execz .LBB3_13
	v_and_b32_e32 v1, 7, v0
	v_add_u32_e32 v15, 1, v1
	v_lshrrev_b32_e32 v5, 5, v0
	s_waitcnt vmcnt(0)
	v_min_u32_e32 v3, 7, v15
	v_add_u32_e32 v10, 1, v5
	v_lshlrev_b32_e32 v9, 2, v3
	v_add_u32_e32 v3, -1, v1
	v_min_u32_e32 v4, 7, v10
	v_mov_b32_e32 v7, 0x4650
	v_max_i32_e32 v13, 0, v3
	v_lshl_add_u32 v4, v4, 5, v7
	v_lshlrev_b32_e32 v6, 2, v1
	v_lshlrev_b32_e32 v18, 2, v13
	v_add_u32_e32 v11, v4, v9
	v_add_u32_e32 v12, v4, v6
	v_add_u32_e32 v13, v4, v18
	v_and_b32_e32 v4, 0xe0, v0
	v_add_u32_e32 v4, 0x4650, v4
	v_add_u32_e32 v14, v4, v9
	v_add_u32_e32 v16, v4, v6
	v_add_u32_e32 v17, v4, v18
	v_add_u32_e32 v4, -1, v5
	v_max_i32_e32 v19, 0, v4
	v_lshl_add_u32 v19, v19, 5, v7
	v_add_u32_e32 v7, v19, v9
	v_bfe_u32 v2, v0, 3, 2
	v_add_u32_e32 v9, v19, v6
	ds_read_b32 v11, v11
	ds_read_b32 v12, v12
	ds_read_b32 v13, v13
	ds_read_b32 v14, v14
	ds_read_b32 v16, v16
	ds_read_b32 v17, v17
	ds_read_b32 v20, v7
	ds_read_b32 v21, v9
	s_waitcnt lgkmcnt(7)
	v_lshrrev_b32_e32 v7, 2, v11
	s_mov_b32 s26, 0x3ffffffc
	v_and_or_b32 v7, v7, s26, v2
	v_lshlrev_b32_e32 v9, 2, v11
	v_mul_lo_u32 v7, v7, 60
	v_and_b32_e32 v9, 60, v9
	v_add3_u32 v7, v9, v7, 4
	v_or_b32_e32 v9, v10, v15
	v_cmp_gt_u32_e32 vcc, 8, v9
	s_waitcnt lgkmcnt(6)
	v_lshrrev_b32_e32 v9, 2, v12
	v_and_or_b32 v9, v9, s26, v2
	v_lshlrev_b32_e32 v11, 2, v12
	v_mul_lo_u32 v9, v9, 60
	v_and_b32_e32 v11, 60, v11
	v_add3_u32 v9, v11, v9, 8
	s_waitcnt lgkmcnt(5)
	v_lshrrev_b32_e32 v11, 2, v13
	v_and_or_b32 v11, v11, s26, v2
	v_lshlrev_b32_e32 v12, 2, v13
	v_mul_lo_u32 v11, v11, 60
	v_and_b32_e32 v12, 60, v12
	v_or_b32_e32 v10, v10, v3
	v_cndmask_b32_e32 v7, 0, v7, vcc
	v_add3_u32 v11, v12, v11, 12
	v_cmp_gt_u32_e32 vcc, 8, v10
	s_waitcnt lgkmcnt(4)
	v_lshlrev_b32_e32 v12, 2, v14
	v_and_b32_e32 v12, 60, v12
	v_cndmask_b32_e32 v10, 0, v11, vcc
	v_lshrrev_b32_e32 v11, 2, v14
	v_and_or_b32 v11, v11, s26, v2
	v_mul_lo_u32 v11, v11, 60
	s_movk_i32 s4, 0xf4
	v_add3_u32 v11, v11, v12, s4
	v_cmp_eq_u32_e32 vcc, 7, v1
	s_movk_i32 s4, 0xfc
	v_cmp_eq_u32_e64 s[6:7], 7, v5
	v_cndmask_b32_e64 v13, v11, 0, vcc
	s_waitcnt lgkmcnt(3)
	v_lshrrev_b32_e32 v11, 2, v16
	v_and_or_b32 v11, v11, s26, v2
	v_mul_lo_u32 v12, v11, 60
	v_lshlrev_b32_e32 v11, 2, v16
	v_and_b32_e32 v14, 60, v11
	s_waitcnt lgkmcnt(2)
	v_lshrrev_b32_e32 v11, 2, v17
	v_and_or_b32 v11, v11, s26, v2
	v_lshlrev_b32_e32 v16, 2, v17
	v_mul_lo_u32 v11, v11, 60
	v_and_b32_e32 v16, 60, v16
	v_add3_u32 v11, v11, v16, s4
	s_waitcnt lgkmcnt(1)
	v_lshrrev_b32_e32 v16, 2, v20
	v_and_or_b32 v16, v16, s26, v2
	v_lshlrev_b32_e32 v20, 2, v20
	v_cndmask_b32_e64 v9, v9, 0, s[6:7]
	v_cndmask_b32_e64 v17, 2, 1, s[6:7]
	v_mul_lo_u32 v16, v16, 60
	v_and_b32_e32 v20, 60, v20
	s_movk_i32 s6, 0x1e4
	v_or_b32_e32 v15, v4, v15
	v_add3_u32 v16, v16, v20, s6
	v_cmp_gt_u32_e64 s[6:7], 8, v15
	s_waitcnt lgkmcnt(0)
	v_lshlrev_b32_e32 v20, 2, v21
	v_and_b32_e32 v20, 60, v20
	v_cndmask_b32_e64 v15, 0, v16, s[6:7]
	v_lshrrev_b32_e32 v16, 2, v21
	v_and_or_b32 v16, v16, s26, v2
	v_mul_lo_u32 v16, v16, 60
	s_movk_i32 s6, 0x1e8
	v_add_u32_e32 v19, v19, v18
	v_cvt_f32_ubyte0_e32 v18, v2
	v_add3_u32 v16, v16, v20, s6
	v_add_f32_e32 v18, 0.5, v18
	v_mov_b32_e32 v20, -0.5
	v_fmamk_f32 v26, v18, 0x3e800000, v20
	v_cmp_gt_f32_e64 s[8:9], 0, v26
	v_sub_u32_e64 v20, v1, 1 clamp
	v_mov_b32_e32 v22, 0x4750
	v_subbrev_co_u32_e64 v18, s[12:13], 0, v5, s[8:9]
	v_cmp_ngt_f32_e64 s[12:13], 0, v26
	v_max_i32_e32 v18, 0, v18
	v_min_u32_e32 v21, 6, v1
	v_addc_co_u32_e64 v5, s[12:13], 0, v5, s[12:13]
	v_min_u32_e32 v5, 7, v5
	v_lshl_add_u32 v18, v18, 5, v22
	v_lshlrev_b32_e32 v20, 2, v20
	v_lshl_add_u32 v5, v5, 5, v22
	v_add_u32_e32 v23, v18, v20
	v_add_u32_e32 v22, v5, v20
	v_lshlrev_b32_e32 v20, 2, v21
	v_add_u32_e32 v24, v18, v6
	v_add_u32_e32 v6, v5, v6
	v_add_u32_e32 v25, v18, v20
	v_add_u32_e32 v5, v5, v20
	v_lshlrev_b32_e32 v18, 1, v7
	ds_read_b32 v19, v19
	ds_read_b32 v20, v23
	ds_read_b32 v22, v22
	ds_read_b32 v21, v24
	ds_read_b32 v23, v6
	ds_read_b32 v24, v25 offset:4
	ds_read_b32 v25, v5 offset:4
	ds_read_b64 v[6:7], v18
	s_waitcnt lgkmcnt(7)
	v_lshrrev_b32_e32 v5, 2, v19
	v_and_or_b32 v2, v5, s26, v2
	v_lshlrev_b32_e32 v5, 2, v19
	v_cmp_gt_u32_e64 s[6:7], 8, v4
	v_mul_lo_u32 v2, v2, 60
	v_and_b32_e32 v5, 60, v5
	s_movk_i32 s12, 0x1ec
	v_cmp_gt_u32_e64 s[4:5], 8, v3
	v_cndmask_b32_e64 v16, 0, v16, s[6:7]
	v_add3_u32 v2, v2, v5, s12
	v_addc_co_u32_e64 v5, s[6:7], 0, v17, s[6:7]
	v_cndmask_b32_e64 v17, 2, 1, vcc
	v_addc_co_u32_e64 v17, vcc, 0, v17, s[4:5]
	v_mul_u32_u24_e32 v5, v5, v17
	v_cvt_f32_ubyte0_e32 v5, v5
	v_cndmask_b32_e64 v11, 0, v11, s[4:5]
	v_div_scale_f32 v17, s[4:5], v5, v5, 1.0
	v_rcp_f32_e32 v19, v17
	v_or_b32_e32 v3, v4, v3
	v_cmp_gt_u32_e32 vcc, 8, v3
	s_mov_b32 s4, 0x3ec00000
	s_mov_b32 s5, 0x3f600000
	v_cndmask_b32_e32 v30, 0, v2, vcc
	v_fma_f32 v2, -v17, v19, 1.0
	v_fmac_f32_e32 v19, v2, v19
	v_div_scale_f32 v2, vcc, 1.0, v5, 1.0
	v_mul_f32_e32 v3, v2, v19
	v_fma_f32 v4, -v17, v3, v2
	v_fmac_f32_e32 v3, v4, v19
	v_fma_f32 v2, -v17, v3, v2
	v_div_fmas_f32 v2, v2, v19, v3
	v_div_fixup_f32 v4, v2, v5, 1.0
	v_add_f32_e32 v2, 1.0, v26
	v_cndmask_b32_e64 v3, v26, v2, s[8:9]
	v_mov_b32_e32 v26, v3
	v_sub_f32_e32 v2, 1.0, v3
	s_waitcnt lgkmcnt(3)
	v_pk_mul_f32 v[22:23], v[26:27], v[22:23] op_sel_hi:[0,1]
	s_waitcnt lgkmcnt(1)
	v_pk_mul_f32 v[24:25], v[2:3], v[24:25]
	v_pk_fma_f32 v[2:3], v[2:3], v[20:21], v[22:23] op_sel_hi:[0,1,1]
	s_mov_b32 s7, 0x3f200000
	s_mov_b32 s6, 0x3e000000
	v_pk_mul_f32 v[20:21], v[2:3], s[4:5]
	v_pk_mul_f32 v[22:23], v[2:3], s[6:7]
	v_pk_add_f32 v[24:25], v[24:25], v[24:25] op_sel:[0,1] op_sel_hi:[0,1]
	v_pk_fma_f32 v[2:3], v[2:3], s[4:5], v[22:23] op_sel:[0,0,1] op_sel_hi:[1,1,0]
	s_mov_b32 s7, s4
	v_mov_b32_e32 v22, v21
	v_pk_fma_f32 v[20:21], v[24:25], s[6:7], v[22:23]
	s_lshr_b32 s4, s2, 2
	v_lshlrev_b32_e32 v22, 4, v1
	v_lshlrev_b32_e32 v1, 1, v9
	v_lshrrev_b32_e32 v8, 3, v0
	s_and_b32 s4, s4, 0xe0
	s_lshl_b32 s3, s3, 7
	ds_read_b64 v[24:25], v1
	v_or_b32_e32 v8, s4, v8
	s_and_b32 s26, s3, 0x380
	s_movk_i32 s3, 0xf0
	v_pk_mul_f32 v[2:3], v[4:5], v[2:3] op_sel_hi:[0,1]
	v_pk_mul_f32 v[4:5], v[4:5], v[20:21] op_sel_hi:[0,1]
	v_or_b32_e32 v20, s20, v8
	v_lshlrev_b32_e32 v8, 1, v10
	v_add3_u32 v9, v12, v14, s3
	v_lshlrev_b32_e32 v10, 1, v13
	v_lshlrev_b32_e32 v9, 1, v9
	ds_read_b64 v[12:13], v8
	ds_read_b64 v[26:27], v10
	ds_read_b64 v[28:29], v9 offset:16
	s_waitcnt lgkmcnt(3)
	v_pk_add_f16 v6, v6, v24
	v_pk_add_f16 v7, v7, v25
	s_waitcnt lgkmcnt(2)
	v_pk_add_f16 v6, v6, v12
	v_pk_add_f16 v7, v7, v13
	s_waitcnt lgkmcnt(1)
	v_pk_add_f16 v6, v6, v26
	v_pk_add_f16 v7, v7, v27
	v_lshlrev_b32_e32 v12, 1, v11
	s_waitcnt lgkmcnt(0)
	v_pk_add_f16 v19, v7, v29
	v_pk_add_f16 v23, v6, v28
	ds_read_b64 v[6:7], v12
	v_lshlrev_b32_e32 v13, 1, v15
	v_lshlrev_b32_e32 v14, 1, v16
	v_lshlrev_b32_e32 v11, 1, v30
	ds_read_b64 v[16:17], v13
	ds_read_b64 v[24:25], v14
	ds_read_b64 v[26:27], v11
	s_waitcnt lgkmcnt(3)
	v_pk_add_f16 v6, v23, v6
	v_pk_add_f16 v7, v19, v7
	s_mov_b64 s[24:25], s[32:33]
	s_waitcnt lgkmcnt(0)
	v_pk_add_f16 v7, v7, v17
	v_pk_add_f16 v6, v6, v16
	v_pk_add_f16 v7, v7, v25
	v_pk_add_f16 v6, v6, v24
	v_pk_add_f16 v7, v7, v27
	v_pk_add_f16 v6, v6, v26
	v_mov_b32_e32 v21, s21
	v_cvt_f32_f16_e32 v16, v6
	v_cvt_f32_f16_sdwa v17, v6 dst_sel:DWORD dst_unused:UNUSED_PAD src0_sel:WORD_1
	v_cvt_f32_f16_e32 v24, v7
	v_cvt_f32_f16_sdwa v25, v7 dst_sel:DWORD dst_unused:UNUSED_PAD src0_sel:WORD_1
	v_lshlrev_b64 v[20:21], 10, v[20:21]
	s_mov_b32 s27, 0
	v_lshl_add_u64 v[20:21], s[24:25], 0, v[20:21]
	v_lshl_add_u64 v[20:21], v[20:21], 0, s[26:27]
	v_mov_b32_e32 v23, 0
	s_movk_i32 s3, 0x100
	v_lshl_add_u64 v[6:7], v[20:21], 0, v[22:23]
	v_pk_mul_f32 v[20:21], v[2:3], v[16:17]
	v_pk_mul_f32 v[22:23], v[4:5], v[24:25]
	v_cmp_gt_u32_e32 vcc, s3, v0
	global_store_dwordx4 v[6:7], v[20:23], off nt
	s_and_b64 exec, exec, vcc
	s_cbranch_execz .LBB3_13
	ds_read_b64 v[16:17], v18 offset:7208
	ds_read_b64 v[18:19], v1 offset:7208
	ds_read_b64 v[20:21], v8 offset:7208
	ds_read_b64 v[22:23], v10 offset:7208
	v_add_co_u32_e32 v6, vcc, 0x40000, v6
	s_waitcnt lgkmcnt(2)
	v_pk_add_f16 v8, v17, v19
	v_pk_add_f16 v1, v16, v18
	s_waitcnt lgkmcnt(1)
	v_pk_add_f16 v10, v8, v21
	ds_read_b64 v[8:9], v9 offset:7224
	ds_read_b64 v[16:17], v12 offset:7208
	ds_read_b64 v[12:13], v13 offset:7208
	ds_read_b64 v[14:15], v14 offset:7208
	v_pk_add_f16 v1, v1, v20
	s_waitcnt lgkmcnt(4)
	v_pk_add_f16 v10, v10, v23
	v_pk_add_f16 v1, v1, v22
	s_waitcnt lgkmcnt(3)
	v_pk_add_f16 v9, v10, v9
	v_pk_add_f16 v1, v1, v8
	s_waitcnt lgkmcnt(2)
	v_pk_add_f16 v10, v9, v17
	ds_read_b64 v[8:9], v11 offset:7208
	v_pk_add_f16 v1, v1, v16
	s_waitcnt lgkmcnt(2)
	v_pk_add_f16 v10, v10, v13
	v_pk_add_f16 v1, v1, v12
	s_waitcnt lgkmcnt(1)
	v_pk_add_f16 v10, v10, v15
	v_pk_add_f16 v1, v1, v14
	s_waitcnt lgkmcnt(0)
	v_pk_add_f16 v11, v10, v9
	v_pk_add_f16 v1, v1, v8
	v_cvt_f32_f16_e32 v10, v11
	v_cvt_f32_f16_e32 v8, v1
	v_cvt_f32_f16_sdwa v9, v1 dst_sel:DWORD dst_unused:UNUSED_PAD src0_sel:WORD_1
	v_cvt_f32_f16_sdwa v11, v11 dst_sel:DWORD dst_unused:UNUSED_PAD src0_sel:WORD_1
	v_addc_co_u32_e32 v7, vcc, 0, v7, vcc
	v_pk_mul_f32 v[2:3], v[2:3], v[8:9]
	v_pk_mul_f32 v[4:5], v[4:5], v[10:11]
	global_store_dwordx4 v[6:7], v[2:5], off nt

.LBB3_14:
	s_and_b64 vcc, exec, s[4:5]
	s_cbranch_vccz .LBB3_29
	s_add_i32 s3, s2, 0xfffffc00
	s_and_b32 s8, s3, -8
	s_waitcnt lgkmcnt(0)
	s_mov_b64 s[4:5], s[38:39]
	s_load_dwordx2 s[6:7], s[14:15], s8 offset:0x0
	s_lshr_b32 s20, s3, 3
	s_and_saveexec_b64 s[8:9], s[10:11]
	s_cbranch_execz .LBB3_17
	s_waitcnt vmcnt(0)
	v_lshl_or_b32 v2, s20, 6, v0
	v_mov_b32_e32 v3, 0
	v_lshlrev_b64 v[2:3], 2, v[2:3]
	v_lshl_add_u64 v[4:5], s[16:17], 0, v[2:3]
	v_lshl_add_u64 v[2:3], s[18:19], 0, v[2:3]
	global_load_dword v1, v[4:5], off
	global_load_dword v6, v[2:3], off
	v_lshlrev_b32_e32 v2, 2, v0
	v_add_u32_e32 v2, 0x50, v2
	s_waitcnt vmcnt(0)
	ds_write2st64_b32 v2, v1, v6 offset0:70 offset1:71

.LBB3_23:
	s_or_b64 exec, exec, s[4:5]
	v_and_b32_e32 v6, 7, v0
	s_waitcnt vmcnt(0)
	v_lshrrev_b32_e32 v1, 3, v0
	v_add_u32_e32 v15, 1, v6
	v_bfe_u32 v3, v1, 1, 3
	v_min_u32_e32 v2, 7, v15
	v_add_u32_e32 v9, 1, v3
	v_lshlrev_b32_e32 v11, 2, v2
	v_add_u32_e32 v2, -1, v6
	v_min_u32_e32 v4, 7, v9
	v_mov_b32_e32 v5, 0x4650
	v_max_i32_e32 v10, 0, v2
	v_lshl_add_u32 v8, v4, 5, v5
	v_lshlrev_b32_e32 v4, 2, v6
	v_lshlrev_b32_e32 v17, 2, v10
	v_lshl_add_u32 v10, v3, 5, v5
	v_add_u32_e32 v14, v10, v11
	v_add_u32_e32 v16, v10, v4
	v_add_u32_e32 v18, v10, v17
	v_add_u32_e32 v10, -1, v3
	v_max_i32_e32 v19, 0, v10
	v_lshl_add_u32 v19, v19, 5, v5
	v_add_u32_e32 v12, v8, v11
	v_add_u32_e32 v13, v8, v4
	v_add_u32_e32 v8, v8, v17
	v_add_u32_e32 v5, v19, v11
	s_waitcnt lgkmcnt(0)
	s_barrier
	v_bfe_u32 v1, v0, 3, 1
	v_add_u32_e32 v11, v19, v4
	ds_read_b32 v12, v12
	ds_read_b32 v13, v13
	ds_read_b32 v20, v8
	ds_read_b32 v14, v14
	ds_read_b32 v8, v16
	ds_read_b32 v16, v18
	ds_read_b32 v18, v5
	ds_read_b32 v21, v11
	s_waitcnt lgkmcnt(7)
	v_ashrrev_i32_e32 v5, 3, v12
	s_mov_b32 s24, 0x7ffffffe
	v_and_or_b32 v5, v5, s24, v1
	v_lshlrev_b32_e32 v11, 1, v12
	v_mul_lo_u32 v5, v5, 30
	v_and_b32_e32 v11, 30, v11
	v_add3_u32 v5, v11, v5, 2
	v_or_b32_e32 v11, v9, v15
	v_cmp_gt_u32_e32 vcc, 8, v11
	s_waitcnt lgkmcnt(6)
	v_ashrrev_i32_e32 v11, 3, v13
	v_and_or_b32 v11, v11, s24, v1
	v_lshlrev_b32_e32 v12, 1, v13
	v_mul_lo_u32 v11, v11, 30
	v_and_b32_e32 v12, 30, v12
	v_add3_u32 v11, v12, v11, 4
	s_waitcnt lgkmcnt(5)
	v_ashrrev_i32_e32 v12, 3, v20
	v_and_or_b32 v12, v12, s24, v1
	v_lshlrev_b32_e32 v13, 1, v20
	v_mul_lo_u32 v12, v12, 30
	v_and_b32_e32 v13, 30, v13
	v_or_b32_e32 v9, v9, v2
	v_cndmask_b32_e32 v5, 0, v5, vcc
	v_add3_u32 v12, v13, v12, 6
	v_cmp_gt_u32_e32 vcc, 8, v9
	s_waitcnt lgkmcnt(4)
	v_ashrrev_i32_e32 v9, 3, v14
	v_lshlrev_b32_e32 v13, 1, v14
	s_waitcnt lgkmcnt(2)
	v_ashrrev_i32_e32 v14, 3, v16
	v_and_or_b32 v14, v14, s24, v1
	v_lshlrev_b32_e32 v16, 1, v16
	v_mul_lo_u32 v14, v14, 30
	v_and_b32_e32 v16, 30, v16
	s_movk_i32 s6, 0x42
	v_add3_u32 v14, v14, v16, s6
	s_waitcnt lgkmcnt(1)
	v_ashrrev_i32_e32 v16, 3, v18
	v_cmp_eq_u32_e64 s[4:5], 7, v3
	v_and_or_b32 v16, v16, s24, v1
	v_lshlrev_b32_e32 v18, 1, v18
	v_cndmask_b32_e64 v11, v11, 0, s[4:5]
	v_cndmask_b32_e64 v24, 2, 1, s[4:5]
	v_mul_lo_u32 v16, v16, 30
	v_and_b32_e32 v18, 30, v18
	s_movk_i32 s4, 0x7a
	v_or_b32_e32 v15, v10, v15
	v_add3_u32 v16, v16, v18, s4
	v_cmp_gt_u32_e64 s[4:5], 8, v15
	s_waitcnt lgkmcnt(0)
	v_lshlrev_b32_e32 v18, 1, v21
	v_and_b32_e32 v18, 30, v18
	v_cndmask_b32_e64 v15, 0, v16, s[4:5]
	v_ashrrev_i32_e32 v16, 3, v21
	v_and_or_b32 v16, v16, s24, v1
	v_mul_lo_u32 v16, v16, 30
	s_movk_i32 s4, 0x7c
	v_add3_u32 v16, v16, v18, s4
	v_cvt_f32_ubyte0_e32 v18, v1
	v_add_f32_e32 v18, 0.5, v18
	v_fma_f32 v25, v18, 0.5, -0.5
	v_cmp_gt_f32_e64 s[8:9], 0, v25
	v_add_u32_e32 v17, v19, v17
	v_sub_u32_e64 v19, v6, 1 clamp
	v_subbrev_co_u32_e64 v18, s[10:11], 0, v3, s[8:9]
	v_cmp_ngt_f32_e64 s[10:11], 0, v25
	v_max_i32_e32 v18, 0, v18
	v_min_u32_e32 v20, 6, v6
	v_addc_co_u32_e64 v3, s[10:11], 0, v3, s[10:11]
	v_min_u32_e32 v3, 7, v3
	v_mov_b32_e32 v21, 0x4750
	v_lshl_add_u32 v18, v18, 5, v21
	v_lshlrev_b32_e32 v19, 2, v19
	v_lshl_add_u32 v3, v3, 5, v21
	v_lshlrev_b32_e32 v20, 2, v20
	v_add_u32_e32 v22, v18, v19
	v_add_u32_e32 v19, v3, v19
	v_add_u32_e32 v21, v18, v4
	v_add_u32_e32 v4, v3, v4
	v_add_u32_e32 v3, v3, v20
	v_and_or_b32 v9, v9, s24, v1
	v_add_u32_e32 v26, v18, v20
	ds_read_b32 v17, v17
	ds_read_b32 v18, v22
	ds_read_b32 v20, v19
	ds_read_b32 v22, v21
	ds_read_b32 v23, v4
	ds_read_b32 v19, v26 offset:4
	ds_read_b32 v21, v3 offset:4
	s_waitcnt lgkmcnt(6)
	v_ashrrev_i32_e32 v3, 3, v17
	v_cndmask_b32_e32 v12, 0, v12, vcc
	v_mul_lo_u32 v9, v9, 30
	v_and_b32_e32 v13, 30, v13
	v_cmp_eq_u32_e32 vcc, 7, v6
	v_and_or_b32 v3, v3, s24, v1
	v_lshlrev_b32_e32 v4, 1, v17
	v_add3_u32 v9, v9, v13, 62
	v_cmp_gt_u32_e64 s[6:7], 8, v2
	v_cmp_gt_u32_e64 s[4:5], 8, v10
	v_mul_lo_u32 v3, v3, 30
	v_and_b32_e32 v4, 30, v4
	s_movk_i32 s10, 0x7e
	v_cndmask_b32_e64 v17, 2, 1, vcc
	v_cndmask_b32_e64 v13, v9, 0, vcc
	v_cndmask_b32_e64 v16, 0, v16, s[4:5]
	v_add3_u32 v3, v3, v4, s10
	v_addc_co_u32_e64 v4, s[4:5], 0, v24, s[4:5]
	v_addc_co_u32_e64 v17, vcc, 0, v17, s[6:7]
	v_mul_u32_u24_e32 v4, v4, v17
	v_cvt_f32_ubyte0_e32 v4, v4
	v_div_scale_f32 v17, s[4:5], v4, v4, 1.0
	v_rcp_f32_e32 v24, v17
	v_or_b32_e32 v2, v10, v2
	v_cmp_gt_u32_e32 vcc, 8, v2
	s_mov_b64 s[12:13], s[34:35]
	v_fma_f32 v2, -v17, v24, 1.0
	v_cndmask_b32_e32 v26, 0, v3, vcc
	v_fmac_f32_e32 v24, v2, v24
	v_div_scale_f32 v2, vcc, 1.0, v4, 1.0
	v_mul_f32_e32 v3, v2, v24
	v_fma_f32 v10, -v17, v3, v2
	v_fmac_f32_e32 v3, v10, v24
	v_fma_f32 v2, -v17, v3, v2
	v_div_fmas_f32 v2, v2, v24, v3
	v_add_f32_e32 v3, 1.0, v25
	v_cndmask_b32_e64 v25, v25, v3, s[8:9]
	v_sub_f32_e32 v24, 1.0, v25
	s_waitcnt lgkmcnt(0)
	v_pk_mul_f32 v[22:23], v[24:25], v[22:23]
	v_mov_b32_e32 v10, v25
	v_add_f32_e32 v3, v22, v23
	v_pk_mul_f32 v[20:21], v[10:11], v[20:21] op_sel_hi:[0,1]
	v_div_fixup_f32 v2, v2, v4, 1.0
	v_mul_f32_e32 v4, 0x3f400000, v3
	v_pk_fma_f32 v[18:19], v[24:25], v[18:19], v[20:21] op_sel_hi:[0,1,1]
	s_mov_b32 s4, 0x3e800000
	v_pk_fma_f32 v[18:19], v[18:19], s[4:5], v[4:5] op_sel_hi:[1,0,0]
	v_cndmask_b32_e64 v14, 0, v14, s[6:7]
	v_pk_mul_f32 v[2:3], v[2:3], v[18:19] op_sel_hi:[0,1]
	s_lshr_b32 s4, s2, 2
	v_lshrrev_b32_e32 v19, 7, v0
	v_bfe_u32 v7, v0, 3, 4
	s_mov_b32 s21, 0
	v_ashrrev_i32_e32 v9, 3, v8
	s_and_b32 s8, s4, 0x70
	v_xor_b32_e32 v18, 7, v19
	s_mov_b64 s[6:7], 0
	v_lshlrev_b32_e32 v10, 1, v5
	v_lshlrev_b32_e32 v11, 1, v11
	v_lshlrev_b32_e32 v12, 1, v12
	v_lshlrev_b32_e32 v13, 1, v13
	v_lshlrev_b32_e32 v14, 1, v14
	v_lshlrev_b32_e32 v15, 1, v15
	v_lshlrev_b32_e32 v16, 1, v16
	v_lshlrev_b32_e32 v17, 1, v26
	s_and_saveexec_b64 s[4:5], s[6:7]
	s_cbranch_execz .LBB3_25
	s_mov_b32 s6, 0x3ffffffe
	v_and_or_b32 v4, v9, s6, v1
	s_or_b32 s6, s8, s23
	v_mul_lo_u32 v22, v4, 60
	v_or_b32_e32 v4, s6, v7
	v_lshlrev_b32_e32 v4, 9, v4
	v_mov_b32_e32 v5, 0
	s_lshl_b32 s6, s20, 6
	v_lshlrev_b32_e32 v23, 2, v8
	v_lshl_add_u64 v[20:21], s[12:13], 0, v[4:5]
	s_and_b32 s20, s6, 0x1c0
	s_movk_i32 s6, 0x70c
	v_mul_u32_u24_e32 v4, 0x70c, v19
	v_and_b32_e32 v23, 60, v23
	v_add3_u32 v4, v4, v23, v22
	v_mad_u32_u24 v22, v19, s6, v10
	v_mad_u32_u24 v23, v19, s6, v11
	v_mad_u32_u24 v24, v19, s6, v12
	v_mad_u32_u24 v25, v19, s6, v13
	v_mad_u32_u24 v26, v19, s6, v14
	v_mad_u32_u24 v27, v19, s6, v15
	v_mad_u32_u24 v28, v19, s6, v16
	ds_read_b32 v22, v22
	ds_read_b32 v23, v23
	ds_read_b32 v24, v24
	ds_read_b32 v25, v25
	ds_read_b32 v26, v26
	ds_read_b32 v27, v27
	ds_read_b32 v28, v28
	ds_read_b32 v4, v4 offset:128
	s_waitcnt lgkmcnt(6)
	v_pk_add_f16 v22, v22, v23
	v_mad_u32_u24 v23, v19, s6, v17
	s_waitcnt lgkmcnt(5)
	v_pk_add_f16 v22, v22, v24
	ds_read_b32 v23, v23
	s_waitcnt lgkmcnt(5)
	v_pk_add_f16 v22, v22, v25
	v_lshl_add_u64 v[20:21], v[20:21], 0, s[20:21]
	s_waitcnt lgkmcnt(1)
	v_pk_add_f16 v4, v22, v4
	s_nop 0
	v_pk_add_f16 v4, v4, v26
	s_nop 0
	v_pk_add_f16 v4, v4, v27
	s_nop 0
	v_pk_add_f16 v4, v4, v28
	s_waitcnt lgkmcnt(0)
	v_pk_add_f16 v4, v4, v23
	s_nop 0
	v_cvt_f32_f16_e32 v22, v4
	v_cvt_f32_f16_sdwa v23, v4 dst_sel:DWORD dst_unused:UNUSED_PAD src0_sel:WORD_1
	v_lshlrev_b32_e32 v4, 3, v6
	v_lshl_add_u64 v[20:21], v[20:21], 0, v[4:5]
	v_lshlrev_b32_e32 v4, 16, v19
	v_pk_mul_f32 v[22:23], v[2:3], v[22:23]
	v_lshl_add_u64 v[4:5], v[20:21], 0, v[4:5]
	v_or_b32_e32 v19, 2, v19
	global_store_dwordx2 v[4:5], v[22:23], off nt

.LBB3_32:
	s_ashr_i32 s12, s2, 3
	s_lshl_b32 s6, s12, 1
	s_ashr_i32 s7, s6, 31
	s_lshl_b64 s[6:7], s[6:7], 2
	s_waitcnt lgkmcnt(0)
	s_add_u32 s8, s14, s6
	s_addc_u32 s9, s15, s7
	s_mov_b64 s[4:5], s[30:31]
	s_load_dwordx2 s[6:7], s[8:9], 0x0
	v_cmp_gt_u32_e32 vcc, 64, v0
	v_lshlrev_b32_e32 v1, 2, v0
	s_and_saveexec_b64 s[8:9], vcc
	s_cbranch_execz .LBB3_34
	s_waitcnt vmcnt(0)
	v_lshl_or_b32 v2, s12, 6, v0
	v_ashrrev_i32_e32 v3, 31, v2
	v_lshlrev_b64 v[2:3], 2, v[2:3]
	v_lshl_add_u64 v[4:5], s[16:17], 0, v[2:3]
	v_lshl_add_u64 v[2:3], s[18:19], 0, v[2:3]
	global_load_dword v6, v[4:5], off
	global_load_dword v7, v[2:3], off
	v_add_u32_e32 v2, 0x50, v1
	s_waitcnt vmcnt(0)
	ds_write2st64_b32 v2, v6, v7 offset0:70 offset1:71

.LBB3_40:
	s_or_b64 exec, exec, s[6:7]
	s_mov_b64 s[10:11], s[28:29]
	s_movk_i32 s0, 0x84
	v_cmp_gt_u32_e32 vcc, s0, v0
	s_and_saveexec_b64 s[0:1], vcc
	s_cbranch_execz .LBB3_42
	v_or_b32_e32 v1, 0x300, v0
	v_min_u32_e32 v3, 0x383, v1
	v_mul_u32_u24_e32 v5, 0x445, v3
	v_mov_b32_e32 v6, 49
	v_lshrrev_b32_e32 v4, 2, v3
	v_mul_lo_u16_sdwa v5, v5, v6 dst_sel:DWORD dst_unused:UNUSED_PAD src0_sel:WORD_1 src1_sel:DWORD
	v_add_lshl_u32 v4, v4, v5, 9
	v_mov_b32_e32 v5, 0
	v_lshlrev_b32_e32 v3, 4, v3
	v_lshl_add_u64 v[6:7], s[4:5], 0, v[4:5]
	v_and_b32_e32 v4, 48, v3
	v_lshl_add_u64 v[4:5], v[6:7], 0, v[4:5]
	global_load_dwordx4 v[4:7], v[4:5], off
	v_lshrrev_b32_e32 v1, 2, v1
	s_movk_i32 s3, 0x50
	v_mad_u32_u24 v1, v1, s3, v2
	s_waitcnt vmcnt(0)
	ds_write_b128 v1, v[4:7]

	.amdhsa_kernel _Z10k_transferPKtS0_PKfPKiS2_S4_PfS5_S5_
		.amdhsa_group_segment_fixed_size 18512
		.amdhsa_private_segment_fixed_size 0
		.amdhsa_kernarg_size 72
		.amdhsa_user_sgpr_count 2
		.amdhsa_user_sgpr_dispatch_ptr 0
		.amdhsa_user_sgpr_queue_ptr 0
		.amdhsa_user_sgpr_kernarg_segment_ptr 1
		.amdhsa_user_sgpr_dispatch_id 0
		.amdhsa_user_sgpr_kernarg_preload_length 0
		.amdhsa_user_sgpr_kernarg_preload_offset 0
		.amdhsa_user_sgpr_private_segment_size 0
		.amdhsa_uses_dynamic_stack 0
		.amdhsa_enable_private_segment 0
		.amdhsa_system_sgpr_workgroup_id_x 1
		.amdhsa_system_sgpr_workgroup_id_y 0
		.amdhsa_system_sgpr_workgroup_id_z 0
		.amdhsa_system_sgpr_workgroup_info 0
		.amdhsa_system_vgpr_workitem_id 0
		.amdhsa_next_free_vgpr 49
		.amdhsa_next_free_sgpr 40
		.amdhsa_accum_offset 52
		.amdhsa_reserve_vcc 1
		.amdhsa_float_round_mode_32 0
		.amdhsa_float_round_mode_16_64 0
		.amdhsa_float_denorm_mode_32 3
		.amdhsa_float_denorm_mode_16_64 3
		.amdhsa_dx10_clamp 1
		.amdhsa_ieee_mode 1
		.amdhsa_fp16_overflow 0
		.amdhsa_tg_split 0
		.amdhsa_exception_fp_ieee_invalid_op 0
		.amdhsa_exception_fp_denorm_src 0
		.amdhsa_exception_fp_ieee_div_zero 0
		.amdhsa_exception_fp_ieee_overflow 0
		.amdhsa_exception_fp_ieee_underflow 0
		.amdhsa_exception_fp_ieee_inexact 0
		.amdhsa_exception_int_div_zero 0
	.end_amdhsa_kernel

amdhsa.kernels:
  - .agpr_count:     0
    .args:
      - .actual_access:  read_only
        .address_space:  global
        .offset:         0
        .size:           8
        .value_kind:     global_buffer
      - .actual_access:  read_only
        .address_space:  global
        .offset:         8
        .size:           8
        .value_kind:     global_buffer
      - .actual_access:  write_only
        .address_space:  global
        .offset:         16
        .size:           8
        .value_kind:     global_buffer
      - .actual_access:  write_only
        .address_space:  global
        .offset:         24
        .size:           8
        .value_kind:     global_buffer
      - .actual_access:  write_only
        .address_space:  global
        .offset:         32
        .size:           8
        .value_kind:     global_buffer
      - .actual_access:  write_only
        .address_space:  global
        .offset:         40
        .size:           8
        .value_kind:     global_buffer
      - .actual_access:  write_only
        .address_space:  global
        .offset:         48
        .size:           8
        .value_kind:     global_buffer
      - .actual_access:  write_only
        .address_space:  global
        .offset:         56
        .size:           8
        .value_kind:     global_buffer
      - .actual_access:  write_only
        .address_space:  global
        .offset:         64
        .size:           8
        .value_kind:     global_buffer
    .group_segment_fixed_size: 18944
    .kernarg_segment_align: 8
    .kernarg_segment_size: 72
    .language:       OpenCL C
    .language_version:
      - 2
      - 0
    .max_flat_workgroup_size: 256
    .name:           _Z6k_prepPKfS0_PfS1_PdS2_PtS3_S3_
    .private_segment_fixed_size: 0
    .sgpr_count:     38
    .sgpr_spill_count: 0
    .symbol:         _Z6k_prepPKfS0_PfS1_PdS2_PtS3_S3_.kd
    .uniform_work_group_size: 1
    .uses_dynamic_stack: false
    .vgpr_count:     29
    .vgpr_spill_count: 0
    .wavefront_size: 64
  - .agpr_count:     16
    .args:
      - .actual_access:  read_only
        .address_space:  global
        .offset:         0
        .size:           8
        .value_kind:     global_buffer
      - .actual_access:  read_only
        .address_space:  global
        .offset:         8
        .size:           8
        .value_kind:     global_buffer
      - .actual_access:  read_only
        .address_space:  global
        .offset:         16
        .size:           8
        .value_kind:     global_buffer
      - .actual_access:  read_only
        .address_space:  global
        .offset:         24
        .size:           8
        .value_kind:     global_buffer
      - .actual_access:  write_only
        .address_space:  global
        .offset:         32
        .size:           8
        .value_kind:     global_buffer
    .group_segment_fixed_size: 256
    .kernarg_segment_align: 8
    .kernarg_segment_size: 40
    .language:       OpenCL C
    .language_version:
      - 2
      - 0
    .max_flat_workgroup_size: 256
    .name:           _Z9k_coarse2PKtS0_PKdS2_Pf
    .private_segment_fixed_size: 0
    .sgpr_count:     46
    .sgpr_spill_count: 0
    .symbol:         _Z9k_coarse2PKtS0_PKdS2_Pf.kd
    .uniform_work_group_size: 1
    .uses_dynamic_stack: false
    .vgpr_count:     156
    .vgpr_spill_count: 0
    .wavefront_size: 64
  - .agpr_count:     0
    .args:
      - .actual_access:  read_only
        .address_space:  global
        .offset:         0
        .size:           8
        .value_kind:     global_buffer
      - .actual_access:  read_only
        .address_space:  global
        .offset:         8
        .size:           8
        .value_kind:     global_buffer
      - .actual_access:  read_only
        .address_space:  global
        .offset:         16
        .size:           8
        .value_kind:     global_buffer
      - .actual_access:  read_only
        .address_space:  global
        .offset:         24
        .size:           8
        .value_kind:     global_buffer
      - .actual_access:  read_only
        .address_space:  global
        .offset:         32
        .size:           8
        .value_kind:     global_buffer
      - .actual_access:  read_only
        .address_space:  global
        .offset:         40
        .size:           8
        .value_kind:     global_buffer
      - .actual_access:  read_only
        .address_space:  global
        .offset:         48
        .size:           8
        .value_kind:     global_buffer
      - .actual_access:  write_only
        .address_space:  global
        .offset:         56
        .size:           8
        .value_kind:     global_buffer
      - .actual_access:  write_only
        .address_space:  global
        .offset:         64
        .size:           8
        .value_kind:     global_buffer
      - .actual_access:  write_only
        .address_space:  global
        .offset:         72
        .size:           8
        .value_kind:     global_buffer
      - .actual_access:  read_only
        .address_space:  global
        .offset:         80
        .size:           8
        .value_kind:     global_buffer
      - .actual_access:  read_only
        .address_space:  global
        .offset:         88
        .size:           8
        .value_kind:     global_buffer
      - .actual_access:  write_only
        .address_space:  global
        .offset:         96
        .size:           8
        .value_kind:     global_buffer
      - .actual_access:  write_only
        .address_space:  global
        .offset:         104
        .size:           8
        .value_kind:     global_buffer
    .group_segment_fixed_size: 30768
    .kernarg_segment_align: 8
    .kernarg_segment_size: 112
    .language:       OpenCL C
    .language_version:
      - 2
      - 0
    .max_flat_workgroup_size: 512
    .name:           _Z7k_fine3PKfS0_PKtS2_PKdS4_S0_PiPfS5_S0_S0_PtS7_
    .private_segment_fixed_size: 0
    .sgpr_count:     106
    .sgpr_spill_count: 4
    .symbol:         _Z7k_fine3PKfS0_PKtS2_PKdS4_S0_PiPfS5_S0_S0_PtS7_.kd
    .uniform_work_group_size: 1
    .uses_dynamic_stack: false
    .vgpr_count:     256
    .vgpr_spill_count: 0
    .wavefront_size: 64
  - .agpr_count:     0
    .args:
      - .actual_access:  read_only
        .address_space:  global
        .offset:         0
        .size:           8
        .value_kind:     global_buffer
      - .actual_access:  read_only
        .address_space:  global
        .offset:         8
        .size:           8
        .value_kind:     global_buffer
      - .actual_access:  read_only
        .address_space:  global
        .offset:         16
        .size:           8
        .value_kind:     global_buffer
      - .actual_access:  read_only
        .address_space:  global
        .offset:         24
        .size:           8
        .value_kind:     global_buffer
      - .actual_access:  read_only
        .address_space:  global
        .offset:         32
        .size:           8
        .value_kind:     global_buffer
      - .actual_access:  read_only
        .address_space:  global
        .offset:         40
        .size:           8
        .value_kind:     global_buffer
      - .actual_access:  write_only
        .address_space:  global
        .offset:         48
        .size:           8
        .value_kind:     global_buffer
      - .actual_access:  write_only
        .address_space:  global
        .offset:         56
        .size:           8
        .value_kind:     global_buffer
      - .actual_access:  write_only
        .address_space:  global
        .offset:         64
        .size:           8
        .value_kind:     global_buffer
    .group_segment_fixed_size: 18512
    .kernarg_segment_align: 8
    .kernarg_segment_size: 72
    .language:       OpenCL C
    .language_version:
      - 2
      - 0
    .max_flat_workgroup_size: 256
    .name:           _Z10k_transferPKtS0_PKfPKiS2_S4_PfS5_S5_
    .private_segment_fixed_size: 0
    .sgpr_count:     46
    .sgpr_spill_count: 0
    .symbol:         _Z10k_transferPKtS0_PKfPKiS2_S4_PfS5_S5_.kd
    .uniform_work_group_size: 1
    .uses_dynamic_stack: false
    .vgpr_count:     49
    .vgpr_spill_count: 0
    .wavefront_size: 64
